# select v5 with the rows walked longest-first (descending groups): the score rows written last in P5 are read first
# speedup vs baseline: 1.0023x; 1.0023x over previous
.LBB0_1220:
	s_waitcnt lgkmcnt(0)
	s_barrier
	s_cmpk_gt_i32 s3, 0x1fff
	s_cbranch_scc1 .LBB0_1868
	s_add_u32 s46, s30, 0x17100000
	s_addc_u32 s47, s31, 0
	s_add_u32 s48, s30, 0x69b00000
	s_addc_u32 s49, s31, 0
	s_add_u32 s50, s30, 0x6a300000
	s_addc_u32 s51, s31, 0
	s_add_i32 s52, s2, 0
	s_cmpk_eq_i32 s84, 0x100
	s_waitcnt vmcnt(11)
	v_lshlrev_b64 v[2:3], v50, -1
	s_cselect_b64 s[18:19], -1, 0
	s_abs_i32 s54, s35
	v_not_b32_e32 v52, v2
	v_cvt_f32_u32_e32 v2, s54
	s_sub_i32 s2, 0, s54
	v_mov_b32_e32 v59, 0
	v_lshlrev_b32_e32 v54, 4, v50
	v_rcp_iflag_f32_e32 v2, v2
	v_mov_b32_e32 v55, v59
	v_not_b32_e32 v1, v3
	v_lshlrev_b32_e32 v56, 2, v50
	v_mul_f32_e32 v2, 0x4f7ffffe, v2
	v_cvt_u32_f32_e32 v2, v2
	v_mov_b32_e32 v57, v59
	s_mov_b64 s[4:5], 0x17100000
	v_lshlrev_b32_e32 v4, 7, v50
	v_readfirstlane_b32 s6, v2
	s_mul_i32 s2, s2, s6
	s_mul_hi_u32 s2, s6, s2
	s_add_i32 s56, s6, s2
	v_lshl_add_u64 v[2:3], s[30:31], 0, v[54:55]
	s_mov_b64 s[6:7], 0x17101000
	v_lshl_add_u64 v[60:61], v[2:3], 0, s[6:7]
	v_lshl_add_u64 v[2:3], s[30:31], 0, v[56:57]
	v_lshlrev_b32_e32 v53, 5, v50
	v_lshlrev_b32_e32 v5, 6, v50
	v_lshl_add_u64 v[62:63], v[2:3], 0, s[4:5]
	v_add_u32_e32 v2, s52, v56
	s_mov_b32 s12, 0
	s_movk_i32 s53, 0x100
	v_cmp_eq_u32_e64 s[0:1], 0, v50
	v_or_b32_e32 v66, 31, v53
	v_or_b32_e32 v67, 30, v53
	v_or_b32_e32 v68, 29, v53
	v_or_b32_e32 v69, 28, v53
	v_or_b32_e32 v70, 27, v53
	v_or_b32_e32 v71, 26, v53
	v_or_b32_e32 v72, 25, v53
	v_or_b32_e32 v73, 24, v53
	v_or_b32_e32 v74, 23, v53
	v_or_b32_e32 v75, 22, v53
	v_or_b32_e32 v76, 21, v53
	v_or_b32_e32 v77, 20, v53
	v_or_b32_e32 v78, 19, v53
	v_or_b32_e32 v79, 18, v53
	v_or_b32_e32 v80, 17, v53
	v_or_b32_e32 v81, 16, v53
	v_or_b32_e32 v82, 15, v53
	v_or_b32_e32 v83, 14, v53
	v_or_b32_e32 v84, 13, v53
	v_or_b32_e32 v85, 12, v53
	v_or_b32_e32 v86, 11, v53
	v_or_b32_e32 v87, 10, v53
	v_or_b32_e32 v88, 9, v53
	v_or_b32_e32 v89, 8, v53
	v_or_b32_e32 v90, 7, v53
	v_or_b32_e32 v91, 6, v53
	v_or_b32_e32 v92, 5, v53
	v_or_b32_e32 v93, 4, v53
	v_or_b32_e32 v94, 3, v53
	v_or_b32_e32 v95, 2, v53
	v_or_b32_e32 v96, 1, v53
	v_or_b32_e32 v97, 15, v54
	v_or_b32_e32 v98, 14, v54
	v_or_b32_e32 v99, 13, v54
	v_or_b32_e32 v100, 12, v54
	v_or_b32_e32 v101, 11, v54
	v_or_b32_e32 v102, 10, v54
	v_or_b32_e32 v103, 9, v54
	v_or_b32_e32 v104, 8, v54
	v_or_b32_e32 v105, 7, v54
	v_or_b32_e32 v106, 6, v54
	v_or_b32_e32 v107, 5, v54
	v_or_b32_e32 v108, 4, v54
	v_or_b32_e32 v109, 3, v54
	v_or_b32_e32 v110, 2, v54
	v_or_b32_e32 v111, 1, v54
	v_or_b32_e32 v112, 64, v50
	v_or_b32_e32 v113, 0x80, v50
	v_or_b32_e32 v114, 0xc0, v50
	s_ashr_i32 s55, s35, 31
	v_add_u32_e32 v55, 0x2000, v2
	s_movk_i32 s57, 0xff
	v_mov_b32_e32 v57, 1
	s_mov_b64 s[20:21], 0x1000
	s_mov_b64 s[22:23], 0x100
	v_add_u32_e32 v115, s52, v5
	v_lshlrev_b32_e32 v116, 2, v50
	v_add_u32_e32 v117, s52, v4
	s_cmpk_eq_i32 s84, 0x100
	s_cbranch_scc0 .LBB0_1223
	s_and_b32 s4, s3, 7
	s_lshr_b32 s5, s4, 2
	s_lshl_b32 s5, s5, 1
	s_add_i32 s4, s4, s5
	s_and_b32 s4, s4, 3
	s_sub_i32 s4, 3, s4
	s_lshl_b32 s4, s4, 11
	s_add_i32 s3, s3, s4
	s_and_b32 s3, s3, 0x1fff
	s_mov_b32 s99, 4
	s_branch .LBB0_1223
.LBB0_1222:
	s_cmpk_eq_i32 s84, 0x100
	s_cbranch_scc0 .Lsel_latch_plain
	s_add_i32 s3, s3, 0x1800
	s_and_b32 s3, s3, 0x1fff
	s_add_i32 s99, s99, -1
	s_cmp_lg_u32 s99, 0
	s_cbranch_scc1 .LBB0_1223
	s_branch .LBB0_1867
